# qkv four workgroups per CU, A and B DMA issued together after the read barrier (one barrier fewer per super-step)
# speedup vs baseline: 1.0164x; 1.0010x over previous
_Z14k_qkv_temporalPKDF16_S0_PKfPDF16_S3_S3_PfPi:
	s_load_dwordx4 s[36:39], s[0:1], 0x0
	s_load_dwordx2 s[40:41], s[0:1], 0x10
	s_load_dwordx4 s[8:11], s[0:1], 0x30
	s_and_b32 s3, s2, 7
	s_mul_i32 s3, s3, 0x71
	s_lshr_b32 s4, s2, 3
	s_add_u32 s3, s3, s4
	s_and_b32 s22, s3, 7
	s_lshr_b32 s16, s3, 3
	s_mul_i32 s16, s16, 14
	v_lshrrev_b32_e32 v1, 6, v0
	v_and_b32_e32 v92, 15, v0
	v_bfe_u32 v90, v0, 4, 2
	v_lshlrev_b32_e32 v95, 2, v90
	v_lshl_or_b32 v91, v1, 5, v95
	v_bfe_u32 v112, v0, 3, 3
	v_and_b32_e32 v113, 7, v0
	v_lshrrev_b32_e32 v114, 1, v112
	v_and_b32_e32 v115, 1, v1
	v_lshl_or_b32 v114, v115, 2, v114
	v_xor_b32_e32 v114, v113, v114
	v_lshlrev_b32_e32 v114, 4, v114
	v_lshl_or_b32 v115, v1, 3, v112
	s_mov_b32 s42, 0x12492493
	s_movk_i32 s43, 0x627
	s_movk_i32 s44, 0x628
	v_add_u32_e32 v116, 0, v115
	v_min_u32_e32 v116, 0x7d, v116
	v_mul_hi_u32 v112, v116, s42
	v_mul_u32_u24_e32 v113, 14, v112
	v_sub_u32_e32 v113, v116, v113
	v_add_u32_e32 v113, s16, v113
	v_min_u32_e32 v113, s43, v113
	v_mad_u32_u24 v113, v112, s44, v113
	v_lshl_or_b32 v100, v113, 10, v114
	v_add_u32_e32 v116, 32, v115
	v_min_u32_e32 v116, 0x7d, v116
	v_mul_hi_u32 v112, v116, s42
	v_mul_u32_u24_e32 v113, 14, v112
	v_sub_u32_e32 v113, v116, v113
	v_add_u32_e32 v113, s16, v113
	v_min_u32_e32 v113, s43, v113
	v_mad_u32_u24 v113, v112, s44, v113
	v_lshl_or_b32 v101, v113, 10, v114
	v_add_u32_e32 v116, 64, v115
	v_min_u32_e32 v116, 0x7d, v116
	v_mul_hi_u32 v112, v116, s42
	v_mul_u32_u24_e32 v113, 14, v112
	v_sub_u32_e32 v113, v116, v113
	v_add_u32_e32 v113, s16, v113
	v_min_u32_e32 v113, s43, v113
	v_mad_u32_u24 v113, v112, s44, v113
	v_lshl_or_b32 v102, v113, 10, v114
	v_add_u32_e32 v116, 96, v115
	v_min_u32_e32 v116, 0x7d, v116
	v_mul_hi_u32 v112, v116, s42
	v_mul_u32_u24_e32 v113, 14, v112
	v_sub_u32_e32 v113, v116, v113
	v_add_u32_e32 v113, s16, v113
	v_min_u32_e32 v113, s43, v113
	v_mad_u32_u24 v113, v112, s44, v113
	v_lshl_or_b32 v103, v113, 10, v114
	s_lshl_b32 s45, s22, 6
	v_add_u32_e32 v116, s45, v115
	v_lshl_or_b32 v120, v116, 10, v114
	v_lshlrev_b32_e32 v116, 10, v1
	s_nop 0
	v_readfirstlane_b32 s24, v116
	s_add_u32 s25, s24, 0x1000
	s_add_u32 s26, s24, 0x2000
	s_add_u32 s27, s24, 0x3000
	s_add_u32 s28, s24, 0x4000
	s_add_u32 s29, s24, 0x5000
	s_add_u32 s30, s24, 0x6000
	s_add_u32 s31, s24, 0x7000
	s_add_u32 s32, s24, 0x8000
	s_add_u32 s33, s24, 0x9000
	v_lshrrev_b32_e32 v116, 1, v92
	v_xor_b32_e32 v116, v90, v116
	v_lshlrev_b32_e32 v116, 4, v116
	v_lshl_or_b32 v121, v92, 7, v116
	v_xor_b32_e32 v122, 64, v121
	v_lshlrev_b32_e32 v116, 12, v1
	v_add_u32_e32 v93, v116, v121
	v_xor_b32_e32 v94, 64, v93
	v_lshl_add_u32 v117, s22, 6, v92
	v_lshlrev_b32_e32 v117, 2, v117
	v_add_u32_e32 v118, 0x1000, v117
	s_waitcnt lgkmcnt(0)
	s_add_u32 s46, s38, 0x8000
	s_addc_u32 s47, s39, 0
	s_add_u32 s48, s38, 0x80000
	s_addc_u32 s49, s39, 0
	s_add_u32 s50, s38, 0x88000
	s_addc_u32 s51, s39, 0
	s_add_u32 s52, s38, 0x100000
	s_addc_u32 s53, s39, 0
	s_add_u32 s54, s38, 0x108000
	s_addc_u32 s55, s39, 0
	global_load_dword v104, v117, s[40:41] offset:0
	global_load_dword v105, v117, s[40:41] offset:64
	global_load_dword v106, v117, s[40:41] offset:128
	global_load_dword v107, v117, s[40:41] offset:192
	global_load_dword v108, v117, s[40:41] offset:2048
	global_load_dword v109, v117, s[40:41] offset:2112
	global_load_dword v110, v117, s[40:41] offset:2176
	global_load_dword v111, v117, s[40:41] offset:2240
	global_load_dword v112, v118, s[40:41] offset:0
	global_load_dword v113, v118, s[40:41] offset:64
	global_load_dword v114, v118, s[40:41] offset:128
	global_load_dword v115, v118, s[40:41] offset:192
	s_mov_b32 m0, s24
	s_nop 0
	global_load_lds_dwordx4 v100, s[36:37]
	s_mov_b32 m0, s25
	s_nop 0
	global_load_lds_dwordx4 v101, s[36:37]
	s_mov_b32 m0, s26
	s_nop 0
	global_load_lds_dwordx4 v102, s[36:37]
	s_mov_b32 m0, s27
	s_nop 0
	global_load_lds_dwordx4 v103, s[36:37]
	s_add_u32 s36, s36, 0x80
	s_addc_u32 s37, s37, 0
	s_mov_b32 m0, s28
	s_nop 0
	global_load_lds_dwordx4 v120, s[38:39]
	s_mov_b32 m0, s29
	s_nop 0
	global_load_lds_dwordx4 v120, s[46:47]
	s_mov_b32 m0, s30
	s_nop 0
	global_load_lds_dwordx4 v120, s[48:49]
	s_mov_b32 m0, s31
	s_nop 0
	global_load_lds_dwordx4 v120, s[50:51]
	s_mov_b32 m0, s32
	s_nop 0
	global_load_lds_dwordx4 v120, s[52:53]
	s_mov_b32 m0, s33
	s_nop 0
	global_load_lds_dwordx4 v120, s[54:55]
	s_add_u32 s38, s38, 0x80
	s_addc_u32 s39, s39, 0
	s_add_u32 s46, s46, 0x80
	s_addc_u32 s47, s47, 0
	s_add_u32 s48, s48, 0x80
	s_addc_u32 s49, s49, 0
	s_add_u32 s50, s50, 0x80
	s_addc_u32 s51, s51, 0
	s_add_u32 s52, s52, 0x80
	s_addc_u32 s53, s53, 0
	s_add_u32 s54, s54, 0x80
	s_addc_u32 s55, s55, 0
	s_waitcnt vmcnt(10)
	v_mov_b32_e32 v124, v104
	v_mov_b32_e32 v125, v104
	v_mov_b32_e32 v126, v104
	v_mov_b32_e32 v127, v104
	v_mov_b32_e32 v62, v104
	v_mov_b32_e32 v63, v104
	v_mov_b32_e32 v64, v104
	v_mov_b32_e32 v65, v104
	v_mov_b32_e32 v86, v105
	v_mov_b32_e32 v87, v105
	v_mov_b32_e32 v88, v105
	v_mov_b32_e32 v89, v105
	v_mov_b32_e32 v58, v105
	v_mov_b32_e32 v59, v105
	v_mov_b32_e32 v60, v105
	v_mov_b32_e32 v61, v105
	v_mov_b32_e32 v96, v106
	v_mov_b32_e32 v97, v106
	v_mov_b32_e32 v98, v106
	v_mov_b32_e32 v99, v106
	v_mov_b32_e32 v54, v106
	v_mov_b32_e32 v55, v106
	v_mov_b32_e32 v56, v106
	v_mov_b32_e32 v57, v106
	v_mov_b32_e32 v82, v107
	v_mov_b32_e32 v83, v107
	v_mov_b32_e32 v84, v107
	v_mov_b32_e32 v85, v107
	v_mov_b32_e32 v50, v107
	v_mov_b32_e32 v51, v107
	v_mov_b32_e32 v52, v107
	v_mov_b32_e32 v53, v107
	v_mov_b32_e32 v78, v108
	v_mov_b32_e32 v79, v108
	v_mov_b32_e32 v80, v108
	v_mov_b32_e32 v81, v108
	v_mov_b32_e32 v46, v108
	v_mov_b32_e32 v47, v108
	v_mov_b32_e32 v48, v108
	v_mov_b32_e32 v49, v108
	v_mov_b32_e32 v74, v109
	v_mov_b32_e32 v75, v109
	v_mov_b32_e32 v76, v109
	v_mov_b32_e32 v77, v109
	v_mov_b32_e32 v42, v109
	v_mov_b32_e32 v43, v109
	v_mov_b32_e32 v44, v109
	v_mov_b32_e32 v45, v109
	v_mov_b32_e32 v70, v110
	v_mov_b32_e32 v71, v110
	v_mov_b32_e32 v72, v110
	v_mov_b32_e32 v73, v110
	v_mov_b32_e32 v38, v110
	v_mov_b32_e32 v39, v110
	v_mov_b32_e32 v40, v110
	v_mov_b32_e32 v41, v110
	v_mov_b32_e32 v66, v111
	v_mov_b32_e32 v67, v111
	v_mov_b32_e32 v68, v111
	v_mov_b32_e32 v69, v111
	v_mov_b32_e32 v34, v111
	v_mov_b32_e32 v35, v111
	v_mov_b32_e32 v36, v111
	v_mov_b32_e32 v37, v111
	v_mov_b32_e32 v18, v112
	v_mov_b32_e32 v19, v112
	v_mov_b32_e32 v20, v112
	v_mov_b32_e32 v21, v112
	v_mov_b32_e32 v2, v112
	v_mov_b32_e32 v3, v112
	v_mov_b32_e32 v4, v112
	v_mov_b32_e32 v5, v112
	v_mov_b32_e32 v26, v113
	v_mov_b32_e32 v27, v113
	v_mov_b32_e32 v28, v113
	v_mov_b32_e32 v29, v113
	v_mov_b32_e32 v10, v113
	v_mov_b32_e32 v11, v113
	v_mov_b32_e32 v12, v113
	v_mov_b32_e32 v13, v113
	v_mov_b32_e32 v22, v114
	v_mov_b32_e32 v23, v114
	v_mov_b32_e32 v24, v114
	v_mov_b32_e32 v25, v114
	v_mov_b32_e32 v6, v114
	v_mov_b32_e32 v7, v114
	v_mov_b32_e32 v8, v114
	v_mov_b32_e32 v9, v114
	v_mov_b32_e32 v30, v115
	v_mov_b32_e32 v31, v115
	v_mov_b32_e32 v32, v115
	v_mov_b32_e32 v33, v115
	v_mov_b32_e32 v14, v115
	v_mov_b32_e32 v15, v115
	v_mov_b32_e32 v16, v115
	v_mov_b32_e32 v17, v115
	s_waitcnt vmcnt(0)
	s_barrier
	ds_read_b128 v[104:107], v93 offset:0
	ds_read_b128 v[108:111], v93 offset:2048
	ds_read_b128 v[112:115], v121 offset:16384
	ds_read_b128 v[116:119], v121 offset:18432
	s_waitcnt lgkmcnt(1)
	v_mfma_f32_16x16x32_f16 v[124:127], v[104:107], v[112:115], v[124:127]
	v_mfma_f32_16x16x32_f16 v[62:65], v[108:111], v[112:115], v[62:65]
	ds_read_b128 v[112:115], v121 offset:20480
	s_waitcnt lgkmcnt(1)
	v_mfma_f32_16x16x32_f16 v[86:89], v[104:107], v[116:119], v[86:89]
	v_mfma_f32_16x16x32_f16 v[58:61], v[108:111], v[116:119], v[58:61]
	ds_read_b128 v[116:119], v121 offset:22528
	s_waitcnt lgkmcnt(1)
	v_mfma_f32_16x16x32_f16 v[96:99], v[104:107], v[112:115], v[96:99]
	v_mfma_f32_16x16x32_f16 v[54:57], v[108:111], v[112:115], v[54:57]
	ds_read_b128 v[112:115], v121 offset:24576
	s_waitcnt lgkmcnt(1)
	v_mfma_f32_16x16x32_f16 v[82:85], v[104:107], v[116:119], v[82:85]
	v_mfma_f32_16x16x32_f16 v[50:53], v[108:111], v[116:119], v[50:53]
	ds_read_b128 v[116:119], v121 offset:26624
	s_waitcnt lgkmcnt(1)
	v_mfma_f32_16x16x32_f16 v[78:81], v[104:107], v[112:115], v[78:81]
	v_mfma_f32_16x16x32_f16 v[46:49], v[108:111], v[112:115], v[46:49]
	ds_read_b128 v[112:115], v121 offset:28672
	s_waitcnt lgkmcnt(1)
	v_mfma_f32_16x16x32_f16 v[74:77], v[104:107], v[116:119], v[74:77]
	v_mfma_f32_16x16x32_f16 v[42:45], v[108:111], v[116:119], v[42:45]
	ds_read_b128 v[116:119], v121 offset:30720
	s_waitcnt lgkmcnt(1)
	v_mfma_f32_16x16x32_f16 v[70:73], v[104:107], v[112:115], v[70:73]
	v_mfma_f32_16x16x32_f16 v[38:41], v[108:111], v[112:115], v[38:41]
	ds_read_b128 v[112:115], v121 offset:32768
	s_waitcnt lgkmcnt(1)
	v_mfma_f32_16x16x32_f16 v[66:69], v[104:107], v[116:119], v[66:69]
	v_mfma_f32_16x16x32_f16 v[34:37], v[108:111], v[116:119], v[34:37]
	ds_read_b128 v[116:119], v121 offset:34816
	s_waitcnt lgkmcnt(1)
	v_mfma_f32_16x16x32_f16 v[18:21], v[104:107], v[112:115], v[18:21]
	v_mfma_f32_16x16x32_f16 v[2:5], v[108:111], v[112:115], v[2:5]
	ds_read_b128 v[112:115], v121 offset:36864
	s_waitcnt lgkmcnt(1)
	v_mfma_f32_16x16x32_f16 v[26:29], v[104:107], v[116:119], v[26:29]
	v_mfma_f32_16x16x32_f16 v[10:13], v[108:111], v[116:119], v[10:13]
	ds_read_b128 v[116:119], v121 offset:38912
	s_waitcnt lgkmcnt(1)
	v_mfma_f32_16x16x32_f16 v[22:25], v[104:107], v[112:115], v[22:25]
	v_mfma_f32_16x16x32_f16 v[6:9], v[108:111], v[112:115], v[6:9]
	ds_read_b128 v[112:115], v122 offset:16384
	s_waitcnt lgkmcnt(1)
	v_mfma_f32_16x16x32_f16 v[30:33], v[104:107], v[116:119], v[30:33]
	v_mfma_f32_16x16x32_f16 v[14:17], v[108:111], v[116:119], v[14:17]
	ds_read_b128 v[116:119], v122 offset:18432
	ds_read_b128 v[104:107], v94 offset:0
	ds_read_b128 v[108:111], v94 offset:2048
	s_waitcnt lgkmcnt(0)
	v_mfma_f32_16x16x32_f16 v[124:127], v[104:107], v[112:115], v[124:127]
	v_mfma_f32_16x16x32_f16 v[62:65], v[108:111], v[112:115], v[62:65]
	ds_read_b128 v[112:115], v122 offset:20480
	s_waitcnt lgkmcnt(1)
	v_mfma_f32_16x16x32_f16 v[86:89], v[104:107], v[116:119], v[86:89]
	v_mfma_f32_16x16x32_f16 v[58:61], v[108:111], v[116:119], v[58:61]
	ds_read_b128 v[116:119], v122 offset:22528
	s_waitcnt lgkmcnt(1)
	v_mfma_f32_16x16x32_f16 v[96:99], v[104:107], v[112:115], v[96:99]
	v_mfma_f32_16x16x32_f16 v[54:57], v[108:111], v[112:115], v[54:57]
	ds_read_b128 v[112:115], v122 offset:24576
	s_waitcnt lgkmcnt(1)
	v_mfma_f32_16x16x32_f16 v[82:85], v[104:107], v[116:119], v[82:85]
	v_mfma_f32_16x16x32_f16 v[50:53], v[108:111], v[116:119], v[50:53]
	ds_read_b128 v[116:119], v122 offset:26624
	s_waitcnt lgkmcnt(1)
	v_mfma_f32_16x16x32_f16 v[78:81], v[104:107], v[112:115], v[78:81]
	v_mfma_f32_16x16x32_f16 v[46:49], v[108:111], v[112:115], v[46:49]
	ds_read_b128 v[112:115], v122 offset:28672
	s_waitcnt lgkmcnt(1)
	v_mfma_f32_16x16x32_f16 v[74:77], v[104:107], v[116:119], v[74:77]
	v_mfma_f32_16x16x32_f16 v[42:45], v[108:111], v[116:119], v[42:45]
	ds_read_b128 v[116:119], v122 offset:30720
	s_waitcnt lgkmcnt(1)
	v_mfma_f32_16x16x32_f16 v[70:73], v[104:107], v[112:115], v[70:73]
	v_mfma_f32_16x16x32_f16 v[38:41], v[108:111], v[112:115], v[38:41]
	ds_read_b128 v[112:115], v122 offset:32768
	s_waitcnt lgkmcnt(1)
	v_mfma_f32_16x16x32_f16 v[66:69], v[104:107], v[116:119], v[66:69]
	v_mfma_f32_16x16x32_f16 v[34:37], v[108:111], v[116:119], v[34:37]
	ds_read_b128 v[116:119], v122 offset:34816
	s_waitcnt lgkmcnt(1)
	v_mfma_f32_16x16x32_f16 v[18:21], v[104:107], v[112:115], v[18:21]
	v_mfma_f32_16x16x32_f16 v[2:5], v[108:111], v[112:115], v[2:5]
	ds_read_b128 v[112:115], v122 offset:36864
	s_waitcnt lgkmcnt(1)
	v_mfma_f32_16x16x32_f16 v[26:29], v[104:107], v[116:119], v[26:29]
	v_mfma_f32_16x16x32_f16 v[10:13], v[108:111], v[116:119], v[10:13]
	ds_read_b128 v[116:119], v122 offset:38912
	s_waitcnt lgkmcnt(0)
	s_barrier
	s_mov_b32 m0, s24
	s_nop 0
	global_load_lds_dwordx4 v100, s[36:37]
	s_mov_b32 m0, s25
	s_nop 0
	global_load_lds_dwordx4 v101, s[36:37]
	s_mov_b32 m0, s26
	s_nop 0
	global_load_lds_dwordx4 v102, s[36:37]
	s_mov_b32 m0, s27
	s_nop 0
	global_load_lds_dwordx4 v103, s[36:37]
	s_add_u32 s36, s36, 0x80
	s_addc_u32 s37, s37, 0
	s_mov_b32 m0, s28
	s_nop 0
	global_load_lds_dwordx4 v120, s[38:39]
	s_mov_b32 m0, s29
	s_nop 0
	global_load_lds_dwordx4 v120, s[46:47]
	s_mov_b32 m0, s30
	s_nop 0
	global_load_lds_dwordx4 v120, s[48:49]
	s_mov_b32 m0, s31
	s_nop 0
	global_load_lds_dwordx4 v120, s[50:51]
	s_mov_b32 m0, s32
	s_nop 0
	global_load_lds_dwordx4 v120, s[52:53]
	s_mov_b32 m0, s33
	s_nop 0
	global_load_lds_dwordx4 v120, s[54:55]
	s_add_u32 s38, s38, 0x80
	s_addc_u32 s39, s39, 0
	s_add_u32 s46, s46, 0x80
	s_addc_u32 s47, s47, 0
	s_add_u32 s48, s48, 0x80
	s_addc_u32 s49, s49, 0
	s_add_u32 s50, s50, 0x80
	s_addc_u32 s51, s51, 0
	s_add_u32 s52, s52, 0x80
	s_addc_u32 s53, s53, 0
	s_add_u32 s54, s54, 0x80
	s_addc_u32 s55, s55, 0
	s_waitcnt lgkmcnt(1)
	v_mfma_f32_16x16x32_f16 v[22:25], v[104:107], v[112:115], v[22:25]
	v_mfma_f32_16x16x32_f16 v[6:9], v[108:111], v[112:115], v[6:9]
	s_waitcnt lgkmcnt(0)
	v_mfma_f32_16x16x32_f16 v[30:33], v[104:107], v[116:119], v[30:33]
	v_mfma_f32_16x16x32_f16 v[14:17], v[108:111], v[116:119], v[14:17]
	s_waitcnt vmcnt(0)
	s_barrier
	ds_read_b128 v[104:107], v93 offset:0
	ds_read_b128 v[108:111], v93 offset:2048
	ds_read_b128 v[112:115], v121 offset:16384
	ds_read_b128 v[116:119], v121 offset:18432
	s_waitcnt lgkmcnt(1)
	v_mfma_f32_16x16x32_f16 v[124:127], v[104:107], v[112:115], v[124:127]
	v_mfma_f32_16x16x32_f16 v[62:65], v[108:111], v[112:115], v[62:65]
	ds_read_b128 v[112:115], v121 offset:20480
	s_waitcnt lgkmcnt(1)
	v_mfma_f32_16x16x32_f16 v[86:89], v[104:107], v[116:119], v[86:89]
	v_mfma_f32_16x16x32_f16 v[58:61], v[108:111], v[116:119], v[58:61]
	ds_read_b128 v[116:119], v121 offset:22528
	s_waitcnt lgkmcnt(1)
	v_mfma_f32_16x16x32_f16 v[96:99], v[104:107], v[112:115], v[96:99]
	v_mfma_f32_16x16x32_f16 v[54:57], v[108:111], v[112:115], v[54:57]
	ds_read_b128 v[112:115], v121 offset:24576
	s_waitcnt lgkmcnt(1)
	v_mfma_f32_16x16x32_f16 v[82:85], v[104:107], v[116:119], v[82:85]
	v_mfma_f32_16x16x32_f16 v[50:53], v[108:111], v[116:119], v[50:53]
	ds_read_b128 v[116:119], v121 offset:26624
	s_waitcnt lgkmcnt(1)
	v_mfma_f32_16x16x32_f16 v[78:81], v[104:107], v[112:115], v[78:81]
	v_mfma_f32_16x16x32_f16 v[46:49], v[108:111], v[112:115], v[46:49]
	ds_read_b128 v[112:115], v121 offset:28672
	s_waitcnt lgkmcnt(1)
	v_mfma_f32_16x16x32_f16 v[74:77], v[104:107], v[116:119], v[74:77]
	v_mfma_f32_16x16x32_f16 v[42:45], v[108:111], v[116:119], v[42:45]
	ds_read_b128 v[116:119], v121 offset:30720
	s_waitcnt lgkmcnt(1)
	v_mfma_f32_16x16x32_f16 v[70:73], v[104:107], v[112:115], v[70:73]
	v_mfma_f32_16x16x32_f16 v[38:41], v[108:111], v[112:115], v[38:41]
	ds_read_b128 v[112:115], v121 offset:32768
	s_waitcnt lgkmcnt(1)
	v_mfma_f32_16x16x32_f16 v[66:69], v[104:107], v[116:119], v[66:69]
	v_mfma_f32_16x16x32_f16 v[34:37], v[108:111], v[116:119], v[34:37]
	ds_read_b128 v[116:119], v121 offset:34816
	s_waitcnt lgkmcnt(1)
	v_mfma_f32_16x16x32_f16 v[18:21], v[104:107], v[112:115], v[18:21]
	v_mfma_f32_16x16x32_f16 v[2:5], v[108:111], v[112:115], v[2:5]
	ds_read_b128 v[112:115], v121 offset:36864
	s_waitcnt lgkmcnt(1)
	v_mfma_f32_16x16x32_f16 v[26:29], v[104:107], v[116:119], v[26:29]
	v_mfma_f32_16x16x32_f16 v[10:13], v[108:111], v[116:119], v[10:13]
	ds_read_b128 v[116:119], v121 offset:38912
	s_waitcnt lgkmcnt(1)
	v_mfma_f32_16x16x32_f16 v[22:25], v[104:107], v[112:115], v[22:25]
	v_mfma_f32_16x16x32_f16 v[6:9], v[108:111], v[112:115], v[6:9]
	ds_read_b128 v[112:115], v122 offset:16384
	s_waitcnt lgkmcnt(1)
	v_mfma_f32_16x16x32_f16 v[30:33], v[104:107], v[116:119], v[30:33]
	v_mfma_f32_16x16x32_f16 v[14:17], v[108:111], v[116:119], v[14:17]
	ds_read_b128 v[116:119], v122 offset:18432
	ds_read_b128 v[104:107], v94 offset:0
	ds_read_b128 v[108:111], v94 offset:2048
	s_waitcnt lgkmcnt(0)
	v_mfma_f32_16x16x32_f16 v[124:127], v[104:107], v[112:115], v[124:127]
	v_mfma_f32_16x16x32_f16 v[62:65], v[108:111], v[112:115], v[62:65]
	ds_read_b128 v[112:115], v122 offset:20480
	s_waitcnt lgkmcnt(1)
	v_mfma_f32_16x16x32_f16 v[86:89], v[104:107], v[116:119], v[86:89]
	v_mfma_f32_16x16x32_f16 v[58:61], v[108:111], v[116:119], v[58:61]
	ds_read_b128 v[116:119], v122 offset:22528
	s_waitcnt lgkmcnt(1)
	v_mfma_f32_16x16x32_f16 v[96:99], v[104:107], v[112:115], v[96:99]
	v_mfma_f32_16x16x32_f16 v[54:57], v[108:111], v[112:115], v[54:57]
	ds_read_b128 v[112:115], v122 offset:24576
	s_waitcnt lgkmcnt(1)
	v_mfma_f32_16x16x32_f16 v[82:85], v[104:107], v[116:119], v[82:85]
	v_mfma_f32_16x16x32_f16 v[50:53], v[108:111], v[116:119], v[50:53]
	ds_read_b128 v[116:119], v122 offset:26624
	s_waitcnt lgkmcnt(1)
	v_mfma_f32_16x16x32_f16 v[78:81], v[104:107], v[112:115], v[78:81]
	v_mfma_f32_16x16x32_f16 v[46:49], v[108:111], v[112:115], v[46:49]
	ds_read_b128 v[112:115], v122 offset:28672
	s_waitcnt lgkmcnt(1)
	v_mfma_f32_16x16x32_f16 v[74:77], v[104:107], v[116:119], v[74:77]
	v_mfma_f32_16x16x32_f16 v[42:45], v[108:111], v[116:119], v[42:45]
	ds_read_b128 v[116:119], v122 offset:30720
	s_waitcnt lgkmcnt(1)
	v_mfma_f32_16x16x32_f16 v[70:73], v[104:107], v[112:115], v[70:73]
	v_mfma_f32_16x16x32_f16 v[38:41], v[108:111], v[112:115], v[38:41]
	ds_read_b128 v[112:115], v122 offset:32768
	s_waitcnt lgkmcnt(1)
	v_mfma_f32_16x16x32_f16 v[66:69], v[104:107], v[116:119], v[66:69]
	v_mfma_f32_16x16x32_f16 v[34:37], v[108:111], v[116:119], v[34:37]
	ds_read_b128 v[116:119], v122 offset:34816
	s_waitcnt lgkmcnt(1)
	v_mfma_f32_16x16x32_f16 v[18:21], v[104:107], v[112:115], v[18:21]
	v_mfma_f32_16x16x32_f16 v[2:5], v[108:111], v[112:115], v[2:5]
	ds_read_b128 v[112:115], v122 offset:36864
	s_waitcnt lgkmcnt(1)
	v_mfma_f32_16x16x32_f16 v[26:29], v[104:107], v[116:119], v[26:29]
	v_mfma_f32_16x16x32_f16 v[10:13], v[108:111], v[116:119], v[10:13]
	ds_read_b128 v[116:119], v122 offset:38912
	s_waitcnt lgkmcnt(0)
	s_barrier
	s_mov_b32 m0, s24
	s_nop 0
	global_load_lds_dwordx4 v100, s[36:37]
	s_mov_b32 m0, s25
	s_nop 0
	global_load_lds_dwordx4 v101, s[36:37]
	s_mov_b32 m0, s26
	s_nop 0
	global_load_lds_dwordx4 v102, s[36:37]
	s_mov_b32 m0, s27
	s_nop 0
	global_load_lds_dwordx4 v103, s[36:37]
	s_add_u32 s36, s36, 0x80
	s_addc_u32 s37, s37, 0
	s_mov_b32 m0, s28
	s_nop 0
	global_load_lds_dwordx4 v120, s[38:39]
	s_mov_b32 m0, s29
	s_nop 0
	global_load_lds_dwordx4 v120, s[46:47]
	s_mov_b32 m0, s30
	s_nop 0
	global_load_lds_dwordx4 v120, s[48:49]
	s_mov_b32 m0, s31
	s_nop 0
	global_load_lds_dwordx4 v120, s[50:51]
	s_mov_b32 m0, s32
	s_nop 0
	global_load_lds_dwordx4 v120, s[52:53]
	s_mov_b32 m0, s33
	s_nop 0
	global_load_lds_dwordx4 v120, s[54:55]
	s_add_u32 s38, s38, 0x80
	s_addc_u32 s39, s39, 0
	s_add_u32 s46, s46, 0x80
	s_addc_u32 s47, s47, 0
	s_add_u32 s48, s48, 0x80
	s_addc_u32 s49, s49, 0
	s_add_u32 s50, s50, 0x80
	s_addc_u32 s51, s51, 0
	s_add_u32 s52, s52, 0x80
	s_addc_u32 s53, s53, 0
	s_add_u32 s54, s54, 0x80
	s_addc_u32 s55, s55, 0
	s_waitcnt lgkmcnt(1)
	v_mfma_f32_16x16x32_f16 v[22:25], v[104:107], v[112:115], v[22:25]
	v_mfma_f32_16x16x32_f16 v[6:9], v[108:111], v[112:115], v[6:9]
	s_waitcnt lgkmcnt(0)
	v_mfma_f32_16x16x32_f16 v[30:33], v[104:107], v[116:119], v[30:33]
	v_mfma_f32_16x16x32_f16 v[14:17], v[108:111], v[116:119], v[14:17]
	s_waitcnt vmcnt(0)
	s_barrier
	ds_read_b128 v[104:107], v93 offset:0
	ds_read_b128 v[108:111], v93 offset:2048
	ds_read_b128 v[112:115], v121 offset:16384
	ds_read_b128 v[116:119], v121 offset:18432
	s_waitcnt lgkmcnt(1)
	v_mfma_f32_16x16x32_f16 v[124:127], v[104:107], v[112:115], v[124:127]
	v_mfma_f32_16x16x32_f16 v[62:65], v[108:111], v[112:115], v[62:65]
	ds_read_b128 v[112:115], v121 offset:20480
	s_waitcnt lgkmcnt(1)
	v_mfma_f32_16x16x32_f16 v[86:89], v[104:107], v[116:119], v[86:89]
	v_mfma_f32_16x16x32_f16 v[58:61], v[108:111], v[116:119], v[58:61]
	ds_read_b128 v[116:119], v121 offset:22528
	s_waitcnt lgkmcnt(1)
	v_mfma_f32_16x16x32_f16 v[96:99], v[104:107], v[112:115], v[96:99]
	v_mfma_f32_16x16x32_f16 v[54:57], v[108:111], v[112:115], v[54:57]
	ds_read_b128 v[112:115], v121 offset:24576
	s_waitcnt lgkmcnt(1)
	v_mfma_f32_16x16x32_f16 v[82:85], v[104:107], v[116:119], v[82:85]
	v_mfma_f32_16x16x32_f16 v[50:53], v[108:111], v[116:119], v[50:53]
	ds_read_b128 v[116:119], v121 offset:26624
	s_waitcnt lgkmcnt(1)
	v_mfma_f32_16x16x32_f16 v[78:81], v[104:107], v[112:115], v[78:81]
	v_mfma_f32_16x16x32_f16 v[46:49], v[108:111], v[112:115], v[46:49]
	ds_read_b128 v[112:115], v121 offset:28672
	s_waitcnt lgkmcnt(1)
	v_mfma_f32_16x16x32_f16 v[74:77], v[104:107], v[116:119], v[74:77]
	v_mfma_f32_16x16x32_f16 v[42:45], v[108:111], v[116:119], v[42:45]
	ds_read_b128 v[116:119], v121 offset:30720
	s_waitcnt lgkmcnt(1)
	v_mfma_f32_16x16x32_f16 v[70:73], v[104:107], v[112:115], v[70:73]
	v_mfma_f32_16x16x32_f16 v[38:41], v[108:111], v[112:115], v[38:41]
	ds_read_b128 v[112:115], v121 offset:32768
	s_waitcnt lgkmcnt(1)
	v_mfma_f32_16x16x32_f16 v[66:69], v[104:107], v[116:119], v[66:69]
	v_mfma_f32_16x16x32_f16 v[34:37], v[108:111], v[116:119], v[34:37]
	ds_read_b128 v[116:119], v121 offset:34816
	s_waitcnt lgkmcnt(1)
	v_mfma_f32_16x16x32_f16 v[18:21], v[104:107], v[112:115], v[18:21]
	v_mfma_f32_16x16x32_f16 v[2:5], v[108:111], v[112:115], v[2:5]
	ds_read_b128 v[112:115], v121 offset:36864
	s_waitcnt lgkmcnt(1)
	v_mfma_f32_16x16x32_f16 v[26:29], v[104:107], v[116:119], v[26:29]
	v_mfma_f32_16x16x32_f16 v[10:13], v[108:111], v[116:119], v[10:13]
	ds_read_b128 v[116:119], v121 offset:38912
	s_waitcnt lgkmcnt(1)
	v_mfma_f32_16x16x32_f16 v[22:25], v[104:107], v[112:115], v[22:25]
	v_mfma_f32_16x16x32_f16 v[6:9], v[108:111], v[112:115], v[6:9]
	ds_read_b128 v[112:115], v122 offset:16384
	s_waitcnt lgkmcnt(1)
	v_mfma_f32_16x16x32_f16 v[30:33], v[104:107], v[116:119], v[30:33]
	v_mfma_f32_16x16x32_f16 v[14:17], v[108:111], v[116:119], v[14:17]
	ds_read_b128 v[116:119], v122 offset:18432
	ds_read_b128 v[104:107], v94 offset:0
	ds_read_b128 v[108:111], v94 offset:2048
	s_waitcnt lgkmcnt(0)
	v_mfma_f32_16x16x32_f16 v[124:127], v[104:107], v[112:115], v[124:127]
	v_mfma_f32_16x16x32_f16 v[62:65], v[108:111], v[112:115], v[62:65]
	ds_read_b128 v[112:115], v122 offset:20480
	s_waitcnt lgkmcnt(1)
	v_mfma_f32_16x16x32_f16 v[86:89], v[104:107], v[116:119], v[86:89]
	v_mfma_f32_16x16x32_f16 v[58:61], v[108:111], v[116:119], v[58:61]
	ds_read_b128 v[116:119], v122 offset:22528
	s_waitcnt lgkmcnt(1)
	v_mfma_f32_16x16x32_f16 v[96:99], v[104:107], v[112:115], v[96:99]
	v_mfma_f32_16x16x32_f16 v[54:57], v[108:111], v[112:115], v[54:57]
	ds_read_b128 v[112:115], v122 offset:24576
	s_waitcnt lgkmcnt(1)
	v_mfma_f32_16x16x32_f16 v[82:85], v[104:107], v[116:119], v[82:85]
	v_mfma_f32_16x16x32_f16 v[50:53], v[108:111], v[116:119], v[50:53]
	ds_read_b128 v[116:119], v122 offset:26624
	s_waitcnt lgkmcnt(1)
	v_mfma_f32_16x16x32_f16 v[78:81], v[104:107], v[112:115], v[78:81]
	v_mfma_f32_16x16x32_f16 v[46:49], v[108:111], v[112:115], v[46:49]
	ds_read_b128 v[112:115], v122 offset:28672
	s_waitcnt lgkmcnt(1)
	v_mfma_f32_16x16x32_f16 v[74:77], v[104:107], v[116:119], v[74:77]
	v_mfma_f32_16x16x32_f16 v[42:45], v[108:111], v[116:119], v[42:45]
	ds_read_b128 v[116:119], v122 offset:30720
	s_waitcnt lgkmcnt(1)
	v_mfma_f32_16x16x32_f16 v[70:73], v[104:107], v[112:115], v[70:73]
	v_mfma_f32_16x16x32_f16 v[38:41], v[108:111], v[112:115], v[38:41]
	ds_read_b128 v[112:115], v122 offset:32768
	s_waitcnt lgkmcnt(1)
	v_mfma_f32_16x16x32_f16 v[66:69], v[104:107], v[116:119], v[66:69]
	v_mfma_f32_16x16x32_f16 v[34:37], v[108:111], v[116:119], v[34:37]
	ds_read_b128 v[116:119], v122 offset:34816
	s_waitcnt lgkmcnt(1)
	v_mfma_f32_16x16x32_f16 v[18:21], v[104:107], v[112:115], v[18:21]
	v_mfma_f32_16x16x32_f16 v[2:5], v[108:111], v[112:115], v[2:5]
	ds_read_b128 v[112:115], v122 offset:36864
	s_waitcnt lgkmcnt(1)
	v_mfma_f32_16x16x32_f16 v[26:29], v[104:107], v[116:119], v[26:29]
	v_mfma_f32_16x16x32_f16 v[10:13], v[108:111], v[116:119], v[10:13]
	ds_read_b128 v[116:119], v122 offset:38912
	s_waitcnt lgkmcnt(0)
	s_barrier
	s_mov_b32 m0, s24
	s_nop 0
	global_load_lds_dwordx4 v100, s[36:37]
	s_mov_b32 m0, s25
	s_nop 0
	global_load_lds_dwordx4 v101, s[36:37]
	s_mov_b32 m0, s26
	s_nop 0
	global_load_lds_dwordx4 v102, s[36:37]
	s_mov_b32 m0, s27
	s_nop 0
	global_load_lds_dwordx4 v103, s[36:37]
	s_add_u32 s36, s36, 0x80
	s_addc_u32 s37, s37, 0
	s_mov_b32 m0, s28
	s_nop 0
	global_load_lds_dwordx4 v120, s[38:39]
	s_mov_b32 m0, s29
	s_nop 0
	global_load_lds_dwordx4 v120, s[46:47]
	s_mov_b32 m0, s30
	s_nop 0
	global_load_lds_dwordx4 v120, s[48:49]
	s_mov_b32 m0, s31
	s_nop 0
	global_load_lds_dwordx4 v120, s[50:51]
	s_mov_b32 m0, s32
	s_nop 0
	global_load_lds_dwordx4 v120, s[52:53]
	s_mov_b32 m0, s33
	s_nop 0
	global_load_lds_dwordx4 v120, s[54:55]
	s_add_u32 s38, s38, 0x80
	s_addc_u32 s39, s39, 0
	s_add_u32 s46, s46, 0x80
	s_addc_u32 s47, s47, 0
	s_add_u32 s48, s48, 0x80
	s_addc_u32 s49, s49, 0
	s_add_u32 s50, s50, 0x80
	s_addc_u32 s51, s51, 0
	s_add_u32 s52, s52, 0x80
	s_addc_u32 s53, s53, 0
	s_add_u32 s54, s54, 0x80
	s_addc_u32 s55, s55, 0
	s_waitcnt lgkmcnt(1)
	v_mfma_f32_16x16x32_f16 v[22:25], v[104:107], v[112:115], v[22:25]
	v_mfma_f32_16x16x32_f16 v[6:9], v[108:111], v[112:115], v[6:9]
	s_waitcnt lgkmcnt(0)
	v_mfma_f32_16x16x32_f16 v[30:33], v[104:107], v[116:119], v[30:33]
	v_mfma_f32_16x16x32_f16 v[14:17], v[108:111], v[116:119], v[14:17]
	s_waitcnt vmcnt(0)
	s_barrier
	ds_read_b128 v[104:107], v93 offset:0
	ds_read_b128 v[108:111], v93 offset:2048
	ds_read_b128 v[112:115], v121 offset:16384
	ds_read_b128 v[116:119], v121 offset:18432
	s_waitcnt lgkmcnt(1)
	v_mfma_f32_16x16x32_f16 v[124:127], v[104:107], v[112:115], v[124:127]
	v_mfma_f32_16x16x32_f16 v[62:65], v[108:111], v[112:115], v[62:65]
	ds_read_b128 v[112:115], v121 offset:20480
	s_waitcnt lgkmcnt(1)
	v_mfma_f32_16x16x32_f16 v[86:89], v[104:107], v[116:119], v[86:89]
	v_mfma_f32_16x16x32_f16 v[58:61], v[108:111], v[116:119], v[58:61]
	ds_read_b128 v[116:119], v121 offset:22528
	s_waitcnt lgkmcnt(1)
	v_mfma_f32_16x16x32_f16 v[96:99], v[104:107], v[112:115], v[96:99]
	v_mfma_f32_16x16x32_f16 v[54:57], v[108:111], v[112:115], v[54:57]
	ds_read_b128 v[112:115], v121 offset:24576
	s_waitcnt lgkmcnt(1)
	v_mfma_f32_16x16x32_f16 v[82:85], v[104:107], v[116:119], v[82:85]
	v_mfma_f32_16x16x32_f16 v[50:53], v[108:111], v[116:119], v[50:53]
	ds_read_b128 v[116:119], v121 offset:26624
	s_waitcnt lgkmcnt(1)
	v_mfma_f32_16x16x32_f16 v[78:81], v[104:107], v[112:115], v[78:81]
	v_mfma_f32_16x16x32_f16 v[46:49], v[108:111], v[112:115], v[46:49]
	ds_read_b128 v[112:115], v121 offset:28672
	s_waitcnt lgkmcnt(1)
	v_mfma_f32_16x16x32_f16 v[74:77], v[104:107], v[116:119], v[74:77]
	v_mfma_f32_16x16x32_f16 v[42:45], v[108:111], v[116:119], v[42:45]
	ds_read_b128 v[116:119], v121 offset:30720
	s_waitcnt lgkmcnt(1)
	v_mfma_f32_16x16x32_f16 v[70:73], v[104:107], v[112:115], v[70:73]
	v_mfma_f32_16x16x32_f16 v[38:41], v[108:111], v[112:115], v[38:41]
	ds_read_b128 v[112:115], v121 offset:32768
	s_waitcnt lgkmcnt(1)
	v_mfma_f32_16x16x32_f16 v[66:69], v[104:107], v[116:119], v[66:69]
	v_mfma_f32_16x16x32_f16 v[34:37], v[108:111], v[116:119], v[34:37]
	ds_read_b128 v[116:119], v121 offset:34816
	s_waitcnt lgkmcnt(1)
	v_mfma_f32_16x16x32_f16 v[18:21], v[104:107], v[112:115], v[18:21]
	v_mfma_f32_16x16x32_f16 v[2:5], v[108:111], v[112:115], v[2:5]
	ds_read_b128 v[112:115], v121 offset:36864
	s_waitcnt lgkmcnt(1)
	v_mfma_f32_16x16x32_f16 v[26:29], v[104:107], v[116:119], v[26:29]
	v_mfma_f32_16x16x32_f16 v[10:13], v[108:111], v[116:119], v[10:13]
	ds_read_b128 v[116:119], v121 offset:38912
	s_waitcnt lgkmcnt(1)
	v_mfma_f32_16x16x32_f16 v[22:25], v[104:107], v[112:115], v[22:25]
	v_mfma_f32_16x16x32_f16 v[6:9], v[108:111], v[112:115], v[6:9]
	ds_read_b128 v[112:115], v122 offset:16384
	s_waitcnt lgkmcnt(1)
	v_mfma_f32_16x16x32_f16 v[30:33], v[104:107], v[116:119], v[30:33]
	v_mfma_f32_16x16x32_f16 v[14:17], v[108:111], v[116:119], v[14:17]
	ds_read_b128 v[116:119], v122 offset:18432
	ds_read_b128 v[104:107], v94 offset:0
	ds_read_b128 v[108:111], v94 offset:2048
	s_waitcnt lgkmcnt(0)
	v_mfma_f32_16x16x32_f16 v[124:127], v[104:107], v[112:115], v[124:127]
	v_mfma_f32_16x16x32_f16 v[62:65], v[108:111], v[112:115], v[62:65]
	ds_read_b128 v[112:115], v122 offset:20480
	s_waitcnt lgkmcnt(1)
	v_mfma_f32_16x16x32_f16 v[86:89], v[104:107], v[116:119], v[86:89]
	v_mfma_f32_16x16x32_f16 v[58:61], v[108:111], v[116:119], v[58:61]
	ds_read_b128 v[116:119], v122 offset:22528
	s_waitcnt lgkmcnt(1)
	v_mfma_f32_16x16x32_f16 v[96:99], v[104:107], v[112:115], v[96:99]
	v_mfma_f32_16x16x32_f16 v[54:57], v[108:111], v[112:115], v[54:57]
	ds_read_b128 v[112:115], v122 offset:24576
	s_waitcnt lgkmcnt(1)
	v_mfma_f32_16x16x32_f16 v[82:85], v[104:107], v[116:119], v[82:85]
	v_mfma_f32_16x16x32_f16 v[50:53], v[108:111], v[116:119], v[50:53]
	ds_read_b128 v[116:119], v122 offset:26624
	s_waitcnt lgkmcnt(1)
	v_mfma_f32_16x16x32_f16 v[78:81], v[104:107], v[112:115], v[78:81]
	v_mfma_f32_16x16x32_f16 v[46:49], v[108:111], v[112:115], v[46:49]
	ds_read_b128 v[112:115], v122 offset:28672
	s_waitcnt lgkmcnt(1)
	v_mfma_f32_16x16x32_f16 v[74:77], v[104:107], v[116:119], v[74:77]
	v_mfma_f32_16x16x32_f16 v[42:45], v[108:111], v[116:119], v[42:45]
	ds_read_b128 v[116:119], v122 offset:30720
	s_waitcnt lgkmcnt(1)
	v_mfma_f32_16x16x32_f16 v[70:73], v[104:107], v[112:115], v[70:73]
	v_mfma_f32_16x16x32_f16 v[38:41], v[108:111], v[112:115], v[38:41]
	ds_read_b128 v[112:115], v122 offset:32768
	s_waitcnt lgkmcnt(1)
	v_mfma_f32_16x16x32_f16 v[66:69], v[104:107], v[116:119], v[66:69]
	v_mfma_f32_16x16x32_f16 v[34:37], v[108:111], v[116:119], v[34:37]
	ds_read_b128 v[116:119], v122 offset:34816
	s_waitcnt lgkmcnt(1)
	v_mfma_f32_16x16x32_f16 v[18:21], v[104:107], v[112:115], v[18:21]
	v_mfma_f32_16x16x32_f16 v[2:5], v[108:111], v[112:115], v[2:5]
	ds_read_b128 v[112:115], v122 offset:36864
	s_waitcnt lgkmcnt(1)
	v_mfma_f32_16x16x32_f16 v[26:29], v[104:107], v[116:119], v[26:29]
	v_mfma_f32_16x16x32_f16 v[10:13], v[108:111], v[116:119], v[10:13]
	ds_read_b128 v[116:119], v122 offset:38912
	s_waitcnt lgkmcnt(0)
	s_barrier
	s_mov_b32 m0, s24
	s_nop 0
	global_load_lds_dwordx4 v100, s[36:37]
	s_mov_b32 m0, s25
	s_nop 0
	global_load_lds_dwordx4 v101, s[36:37]
	s_mov_b32 m0, s26
	s_nop 0
	global_load_lds_dwordx4 v102, s[36:37]
	s_mov_b32 m0, s27
	s_nop 0
	global_load_lds_dwordx4 v103, s[36:37]
	s_add_u32 s36, s36, 0x80
	s_addc_u32 s37, s37, 0
	s_mov_b32 m0, s28
	s_nop 0
	global_load_lds_dwordx4 v120, s[38:39]
	s_mov_b32 m0, s29
	s_nop 0
	global_load_lds_dwordx4 v120, s[46:47]
	s_mov_b32 m0, s30
	s_nop 0
	global_load_lds_dwordx4 v120, s[48:49]
	s_mov_b32 m0, s31
	s_nop 0
	global_load_lds_dwordx4 v120, s[50:51]
	s_mov_b32 m0, s32
	s_nop 0
	global_load_lds_dwordx4 v120, s[52:53]
	s_mov_b32 m0, s33
	s_nop 0
	global_load_lds_dwordx4 v120, s[54:55]
	s_add_u32 s38, s38, 0x80
	s_addc_u32 s39, s39, 0
	s_add_u32 s46, s46, 0x80
	s_addc_u32 s47, s47, 0
	s_add_u32 s48, s48, 0x80
	s_addc_u32 s49, s49, 0
	s_add_u32 s50, s50, 0x80
	s_addc_u32 s51, s51, 0
	s_add_u32 s52, s52, 0x80
	s_addc_u32 s53, s53, 0
	s_add_u32 s54, s54, 0x80
	s_addc_u32 s55, s55, 0
	s_waitcnt lgkmcnt(1)
	v_mfma_f32_16x16x32_f16 v[22:25], v[104:107], v[112:115], v[22:25]
	v_mfma_f32_16x16x32_f16 v[6:9], v[108:111], v[112:115], v[6:9]
	s_waitcnt lgkmcnt(0)
	v_mfma_f32_16x16x32_f16 v[30:33], v[104:107], v[116:119], v[30:33]
	v_mfma_f32_16x16x32_f16 v[14:17], v[108:111], v[116:119], v[14:17]
	s_waitcnt vmcnt(0)
	s_barrier
	ds_read_b128 v[104:107], v93 offset:0
	ds_read_b128 v[108:111], v93 offset:2048
	ds_read_b128 v[112:115], v121 offset:16384
	ds_read_b128 v[116:119], v121 offset:18432
	s_waitcnt lgkmcnt(1)
	v_mfma_f32_16x16x32_f16 v[124:127], v[104:107], v[112:115], v[124:127]
	v_mfma_f32_16x16x32_f16 v[62:65], v[108:111], v[112:115], v[62:65]
	ds_read_b128 v[112:115], v121 offset:20480
	s_waitcnt lgkmcnt(1)
	v_mfma_f32_16x16x32_f16 v[86:89], v[104:107], v[116:119], v[86:89]
	v_mfma_f32_16x16x32_f16 v[58:61], v[108:111], v[116:119], v[58:61]
	ds_read_b128 v[116:119], v121 offset:22528
	s_waitcnt lgkmcnt(1)
	v_mfma_f32_16x16x32_f16 v[96:99], v[104:107], v[112:115], v[96:99]
	v_mfma_f32_16x16x32_f16 v[54:57], v[108:111], v[112:115], v[54:57]
	ds_read_b128 v[112:115], v121 offset:24576
	s_waitcnt lgkmcnt(1)
	v_mfma_f32_16x16x32_f16 v[82:85], v[104:107], v[116:119], v[82:85]
	v_mfma_f32_16x16x32_f16 v[50:53], v[108:111], v[116:119], v[50:53]
	ds_read_b128 v[116:119], v121 offset:26624
	s_waitcnt lgkmcnt(1)
	v_mfma_f32_16x16x32_f16 v[78:81], v[104:107], v[112:115], v[78:81]
	v_mfma_f32_16x16x32_f16 v[46:49], v[108:111], v[112:115], v[46:49]
	ds_read_b128 v[112:115], v121 offset:28672
	s_waitcnt lgkmcnt(1)
	v_mfma_f32_16x16x32_f16 v[74:77], v[104:107], v[116:119], v[74:77]
	v_mfma_f32_16x16x32_f16 v[42:45], v[108:111], v[116:119], v[42:45]
	ds_read_b128 v[116:119], v121 offset:30720
	s_waitcnt lgkmcnt(1)
	v_mfma_f32_16x16x32_f16 v[70:73], v[104:107], v[112:115], v[70:73]
	v_mfma_f32_16x16x32_f16 v[38:41], v[108:111], v[112:115], v[38:41]
	ds_read_b128 v[112:115], v121 offset:32768
	s_waitcnt lgkmcnt(1)
	v_mfma_f32_16x16x32_f16 v[66:69], v[104:107], v[116:119], v[66:69]
	v_mfma_f32_16x16x32_f16 v[34:37], v[108:111], v[116:119], v[34:37]
	ds_read_b128 v[116:119], v121 offset:34816
	s_waitcnt lgkmcnt(1)
	v_mfma_f32_16x16x32_f16 v[18:21], v[104:107], v[112:115], v[18:21]
	v_mfma_f32_16x16x32_f16 v[2:5], v[108:111], v[112:115], v[2:5]
	ds_read_b128 v[112:115], v121 offset:36864
	s_waitcnt lgkmcnt(1)
	v_mfma_f32_16x16x32_f16 v[26:29], v[104:107], v[116:119], v[26:29]
	v_mfma_f32_16x16x32_f16 v[10:13], v[108:111], v[116:119], v[10:13]
	ds_read_b128 v[116:119], v121 offset:38912
	s_waitcnt lgkmcnt(1)
	v_mfma_f32_16x16x32_f16 v[22:25], v[104:107], v[112:115], v[22:25]
	v_mfma_f32_16x16x32_f16 v[6:9], v[108:111], v[112:115], v[6:9]
	ds_read_b128 v[112:115], v122 offset:16384
	s_waitcnt lgkmcnt(1)
	v_mfma_f32_16x16x32_f16 v[30:33], v[104:107], v[116:119], v[30:33]
	v_mfma_f32_16x16x32_f16 v[14:17], v[108:111], v[116:119], v[14:17]
	ds_read_b128 v[116:119], v122 offset:18432
	ds_read_b128 v[104:107], v94 offset:0
	ds_read_b128 v[108:111], v94 offset:2048
	s_waitcnt lgkmcnt(0)
	v_mfma_f32_16x16x32_f16 v[124:127], v[104:107], v[112:115], v[124:127]
	v_mfma_f32_16x16x32_f16 v[62:65], v[108:111], v[112:115], v[62:65]
	ds_read_b128 v[112:115], v122 offset:20480
	s_waitcnt lgkmcnt(1)
	v_mfma_f32_16x16x32_f16 v[86:89], v[104:107], v[116:119], v[86:89]
	v_mfma_f32_16x16x32_f16 v[58:61], v[108:111], v[116:119], v[58:61]
	ds_read_b128 v[116:119], v122 offset:22528
	s_waitcnt lgkmcnt(1)
	v_mfma_f32_16x16x32_f16 v[96:99], v[104:107], v[112:115], v[96:99]
	v_mfma_f32_16x16x32_f16 v[54:57], v[108:111], v[112:115], v[54:57]
	ds_read_b128 v[112:115], v122 offset:24576
	s_waitcnt lgkmcnt(1)
	v_mfma_f32_16x16x32_f16 v[82:85], v[104:107], v[116:119], v[82:85]
	v_mfma_f32_16x16x32_f16 v[50:53], v[108:111], v[116:119], v[50:53]
	ds_read_b128 v[116:119], v122 offset:26624
	s_waitcnt lgkmcnt(1)
	v_mfma_f32_16x16x32_f16 v[78:81], v[104:107], v[112:115], v[78:81]
	v_mfma_f32_16x16x32_f16 v[46:49], v[108:111], v[112:115], v[46:49]
	ds_read_b128 v[112:115], v122 offset:28672
	s_waitcnt lgkmcnt(1)
	v_mfma_f32_16x16x32_f16 v[74:77], v[104:107], v[116:119], v[74:77]
	v_mfma_f32_16x16x32_f16 v[42:45], v[108:111], v[116:119], v[42:45]
	ds_read_b128 v[116:119], v122 offset:30720
	s_waitcnt lgkmcnt(1)
	v_mfma_f32_16x16x32_f16 v[70:73], v[104:107], v[112:115], v[70:73]
	v_mfma_f32_16x16x32_f16 v[38:41], v[108:111], v[112:115], v[38:41]
	ds_read_b128 v[112:115], v122 offset:32768
	s_waitcnt lgkmcnt(1)
	v_mfma_f32_16x16x32_f16 v[66:69], v[104:107], v[116:119], v[66:69]
	v_mfma_f32_16x16x32_f16 v[34:37], v[108:111], v[116:119], v[34:37]
	ds_read_b128 v[116:119], v122 offset:34816
	s_waitcnt lgkmcnt(1)
	v_mfma_f32_16x16x32_f16 v[18:21], v[104:107], v[112:115], v[18:21]
	v_mfma_f32_16x16x32_f16 v[2:5], v[108:111], v[112:115], v[2:5]
	ds_read_b128 v[112:115], v122 offset:36864
	s_waitcnt lgkmcnt(1)
	v_mfma_f32_16x16x32_f16 v[26:29], v[104:107], v[116:119], v[26:29]
	v_mfma_f32_16x16x32_f16 v[10:13], v[108:111], v[116:119], v[10:13]
	ds_read_b128 v[116:119], v122 offset:38912
	s_waitcnt lgkmcnt(0)
	s_barrier
	s_mov_b32 m0, s24
	s_nop 0
	global_load_lds_dwordx4 v100, s[36:37]
	s_mov_b32 m0, s25
	s_nop 0
	global_load_lds_dwordx4 v101, s[36:37]
	s_mov_b32 m0, s26
	s_nop 0
	global_load_lds_dwordx4 v102, s[36:37]
	s_mov_b32 m0, s27
	s_nop 0
	global_load_lds_dwordx4 v103, s[36:37]
	s_add_u32 s36, s36, 0x80
	s_addc_u32 s37, s37, 0
	s_mov_b32 m0, s28
	s_nop 0
	global_load_lds_dwordx4 v120, s[38:39]
	s_mov_b32 m0, s29
	s_nop 0
	global_load_lds_dwordx4 v120, s[46:47]
	s_mov_b32 m0, s30
	s_nop 0
	global_load_lds_dwordx4 v120, s[48:49]
	s_mov_b32 m0, s31
	s_nop 0
	global_load_lds_dwordx4 v120, s[50:51]
	s_mov_b32 m0, s32
	s_nop 0
	global_load_lds_dwordx4 v120, s[52:53]
	s_mov_b32 m0, s33
	s_nop 0
	global_load_lds_dwordx4 v120, s[54:55]
	s_add_u32 s38, s38, 0x80
	s_addc_u32 s39, s39, 0
	s_add_u32 s46, s46, 0x80
	s_addc_u32 s47, s47, 0
	s_add_u32 s48, s48, 0x80
	s_addc_u32 s49, s49, 0
	s_add_u32 s50, s50, 0x80
	s_addc_u32 s51, s51, 0
	s_add_u32 s52, s52, 0x80
	s_addc_u32 s53, s53, 0
	s_add_u32 s54, s54, 0x80
	s_addc_u32 s55, s55, 0
	s_waitcnt lgkmcnt(1)
	v_mfma_f32_16x16x32_f16 v[22:25], v[104:107], v[112:115], v[22:25]
	v_mfma_f32_16x16x32_f16 v[6:9], v[108:111], v[112:115], v[6:9]
	s_waitcnt lgkmcnt(0)
	v_mfma_f32_16x16x32_f16 v[30:33], v[104:107], v[116:119], v[30:33]
	v_mfma_f32_16x16x32_f16 v[14:17], v[108:111], v[116:119], v[14:17]
	s_waitcnt vmcnt(0)
	s_barrier
	ds_read_b128 v[104:107], v93 offset:0
	ds_read_b128 v[108:111], v93 offset:2048
	ds_read_b128 v[112:115], v121 offset:16384
	ds_read_b128 v[116:119], v121 offset:18432
	s_waitcnt lgkmcnt(1)
	v_mfma_f32_16x16x32_f16 v[124:127], v[104:107], v[112:115], v[124:127]
	v_mfma_f32_16x16x32_f16 v[62:65], v[108:111], v[112:115], v[62:65]
	ds_read_b128 v[112:115], v121 offset:20480
	s_waitcnt lgkmcnt(1)
	v_mfma_f32_16x16x32_f16 v[86:89], v[104:107], v[116:119], v[86:89]
	v_mfma_f32_16x16x32_f16 v[58:61], v[108:111], v[116:119], v[58:61]
	ds_read_b128 v[116:119], v121 offset:22528
	s_waitcnt lgkmcnt(1)
	v_mfma_f32_16x16x32_f16 v[96:99], v[104:107], v[112:115], v[96:99]
	v_mfma_f32_16x16x32_f16 v[54:57], v[108:111], v[112:115], v[54:57]
	ds_read_b128 v[112:115], v121 offset:24576
	s_waitcnt lgkmcnt(1)
	v_mfma_f32_16x16x32_f16 v[82:85], v[104:107], v[116:119], v[82:85]
	v_mfma_f32_16x16x32_f16 v[50:53], v[108:111], v[116:119], v[50:53]
	ds_read_b128 v[116:119], v121 offset:26624
	s_waitcnt lgkmcnt(1)
	v_mfma_f32_16x16x32_f16 v[78:81], v[104:107], v[112:115], v[78:81]
	v_mfma_f32_16x16x32_f16 v[46:49], v[108:111], v[112:115], v[46:49]
	ds_read_b128 v[112:115], v121 offset:28672
	s_waitcnt lgkmcnt(1)
	v_mfma_f32_16x16x32_f16 v[74:77], v[104:107], v[116:119], v[74:77]
	v_mfma_f32_16x16x32_f16 v[42:45], v[108:111], v[116:119], v[42:45]
	ds_read_b128 v[116:119], v121 offset:30720
	s_waitcnt lgkmcnt(1)
	v_mfma_f32_16x16x32_f16 v[70:73], v[104:107], v[112:115], v[70:73]
	v_mfma_f32_16x16x32_f16 v[38:41], v[108:111], v[112:115], v[38:41]
	ds_read_b128 v[112:115], v121 offset:32768
	s_waitcnt lgkmcnt(1)
	v_mfma_f32_16x16x32_f16 v[66:69], v[104:107], v[116:119], v[66:69]
	v_mfma_f32_16x16x32_f16 v[34:37], v[108:111], v[116:119], v[34:37]
	ds_read_b128 v[116:119], v121 offset:34816
	s_waitcnt lgkmcnt(1)
	v_mfma_f32_16x16x32_f16 v[18:21], v[104:107], v[112:115], v[18:21]
	v_mfma_f32_16x16x32_f16 v[2:5], v[108:111], v[112:115], v[2:5]
	ds_read_b128 v[112:115], v121 offset:36864
	s_waitcnt lgkmcnt(1)
	v_mfma_f32_16x16x32_f16 v[26:29], v[104:107], v[116:119], v[26:29]
	v_mfma_f32_16x16x32_f16 v[10:13], v[108:111], v[116:119], v[10:13]
	ds_read_b128 v[116:119], v121 offset:38912
	s_waitcnt lgkmcnt(1)
	v_mfma_f32_16x16x32_f16 v[22:25], v[104:107], v[112:115], v[22:25]
	v_mfma_f32_16x16x32_f16 v[6:9], v[108:111], v[112:115], v[6:9]
	ds_read_b128 v[112:115], v122 offset:16384
	s_waitcnt lgkmcnt(1)
	v_mfma_f32_16x16x32_f16 v[30:33], v[104:107], v[116:119], v[30:33]
	v_mfma_f32_16x16x32_f16 v[14:17], v[108:111], v[116:119], v[14:17]
	ds_read_b128 v[116:119], v122 offset:18432
	ds_read_b128 v[104:107], v94 offset:0
	ds_read_b128 v[108:111], v94 offset:2048
	s_waitcnt lgkmcnt(0)
	v_mfma_f32_16x16x32_f16 v[124:127], v[104:107], v[112:115], v[124:127]
	v_mfma_f32_16x16x32_f16 v[62:65], v[108:111], v[112:115], v[62:65]
	ds_read_b128 v[112:115], v122 offset:20480
	s_waitcnt lgkmcnt(1)
	v_mfma_f32_16x16x32_f16 v[86:89], v[104:107], v[116:119], v[86:89]
	v_mfma_f32_16x16x32_f16 v[58:61], v[108:111], v[116:119], v[58:61]
	ds_read_b128 v[116:119], v122 offset:22528
	s_waitcnt lgkmcnt(1)
	v_mfma_f32_16x16x32_f16 v[96:99], v[104:107], v[112:115], v[96:99]
	v_mfma_f32_16x16x32_f16 v[54:57], v[108:111], v[112:115], v[54:57]
	ds_read_b128 v[112:115], v122 offset:24576
	s_waitcnt lgkmcnt(1)
	v_mfma_f32_16x16x32_f16 v[82:85], v[104:107], v[116:119], v[82:85]
	v_mfma_f32_16x16x32_f16 v[50:53], v[108:111], v[116:119], v[50:53]
	ds_read_b128 v[116:119], v122 offset:26624
	s_waitcnt lgkmcnt(1)
	v_mfma_f32_16x16x32_f16 v[78:81], v[104:107], v[112:115], v[78:81]
	v_mfma_f32_16x16x32_f16 v[46:49], v[108:111], v[112:115], v[46:49]
	ds_read_b128 v[112:115], v122 offset:28672
	s_waitcnt lgkmcnt(1)
	v_mfma_f32_16x16x32_f16 v[74:77], v[104:107], v[116:119], v[74:77]
	v_mfma_f32_16x16x32_f16 v[42:45], v[108:111], v[116:119], v[42:45]
	ds_read_b128 v[116:119], v122 offset:30720
	s_waitcnt lgkmcnt(1)
	v_mfma_f32_16x16x32_f16 v[70:73], v[104:107], v[112:115], v[70:73]
	v_mfma_f32_16x16x32_f16 v[38:41], v[108:111], v[112:115], v[38:41]
	ds_read_b128 v[112:115], v122 offset:32768
	s_waitcnt lgkmcnt(1)
	v_mfma_f32_16x16x32_f16 v[66:69], v[104:107], v[116:119], v[66:69]
	v_mfma_f32_16x16x32_f16 v[34:37], v[108:111], v[116:119], v[34:37]
	ds_read_b128 v[116:119], v122 offset:34816
	s_waitcnt lgkmcnt(1)
	v_mfma_f32_16x16x32_f16 v[18:21], v[104:107], v[112:115], v[18:21]
	v_mfma_f32_16x16x32_f16 v[2:5], v[108:111], v[112:115], v[2:5]
	ds_read_b128 v[112:115], v122 offset:36864
	s_waitcnt lgkmcnt(1)
	v_mfma_f32_16x16x32_f16 v[26:29], v[104:107], v[116:119], v[26:29]
	v_mfma_f32_16x16x32_f16 v[10:13], v[108:111], v[116:119], v[10:13]
	ds_read_b128 v[116:119], v122 offset:38912
	s_waitcnt lgkmcnt(0)
	s_barrier
	s_mov_b32 m0, s24
	s_nop 0
	global_load_lds_dwordx4 v100, s[36:37]
	s_mov_b32 m0, s25
	s_nop 0
	global_load_lds_dwordx4 v101, s[36:37]
	s_mov_b32 m0, s26
	s_nop 0
	global_load_lds_dwordx4 v102, s[36:37]
	s_mov_b32 m0, s27
	s_nop 0
	global_load_lds_dwordx4 v103, s[36:37]
	s_add_u32 s36, s36, 0x80
	s_addc_u32 s37, s37, 0
	s_mov_b32 m0, s28
	s_nop 0
	global_load_lds_dwordx4 v120, s[38:39]
	s_mov_b32 m0, s29
	s_nop 0
	global_load_lds_dwordx4 v120, s[46:47]
	s_mov_b32 m0, s30
	s_nop 0
	global_load_lds_dwordx4 v120, s[48:49]
	s_mov_b32 m0, s31
	s_nop 0
	global_load_lds_dwordx4 v120, s[50:51]
	s_mov_b32 m0, s32
	s_nop 0
	global_load_lds_dwordx4 v120, s[52:53]
	s_mov_b32 m0, s33
	s_nop 0
	global_load_lds_dwordx4 v120, s[54:55]
	s_add_u32 s38, s38, 0x80
	s_addc_u32 s39, s39, 0
	s_add_u32 s46, s46, 0x80
	s_addc_u32 s47, s47, 0
	s_add_u32 s48, s48, 0x80
	s_addc_u32 s49, s49, 0
	s_add_u32 s50, s50, 0x80
	s_addc_u32 s51, s51, 0
	s_add_u32 s52, s52, 0x80
	s_addc_u32 s53, s53, 0
	s_add_u32 s54, s54, 0x80
	s_addc_u32 s55, s55, 0
	s_waitcnt lgkmcnt(1)
	v_mfma_f32_16x16x32_f16 v[22:25], v[104:107], v[112:115], v[22:25]
	v_mfma_f32_16x16x32_f16 v[6:9], v[108:111], v[112:115], v[6:9]
	s_waitcnt lgkmcnt(0)
	v_mfma_f32_16x16x32_f16 v[30:33], v[104:107], v[116:119], v[30:33]
	v_mfma_f32_16x16x32_f16 v[14:17], v[108:111], v[116:119], v[14:17]
	s_waitcnt vmcnt(0)
	s_barrier
	ds_read_b128 v[104:107], v93 offset:0
	ds_read_b128 v[108:111], v93 offset:2048
	ds_read_b128 v[112:115], v121 offset:16384
	ds_read_b128 v[116:119], v121 offset:18432
	s_waitcnt lgkmcnt(1)
	v_mfma_f32_16x16x32_f16 v[124:127], v[104:107], v[112:115], v[124:127]
	v_mfma_f32_16x16x32_f16 v[62:65], v[108:111], v[112:115], v[62:65]
	ds_read_b128 v[112:115], v121 offset:20480
	s_waitcnt lgkmcnt(1)
	v_mfma_f32_16x16x32_f16 v[86:89], v[104:107], v[116:119], v[86:89]
	v_mfma_f32_16x16x32_f16 v[58:61], v[108:111], v[116:119], v[58:61]
	ds_read_b128 v[116:119], v121 offset:22528
	s_waitcnt lgkmcnt(1)
	v_mfma_f32_16x16x32_f16 v[96:99], v[104:107], v[112:115], v[96:99]
	v_mfma_f32_16x16x32_f16 v[54:57], v[108:111], v[112:115], v[54:57]
	ds_read_b128 v[112:115], v121 offset:24576
	s_waitcnt lgkmcnt(1)
	v_mfma_f32_16x16x32_f16 v[82:85], v[104:107], v[116:119], v[82:85]
	v_mfma_f32_16x16x32_f16 v[50:53], v[108:111], v[116:119], v[50:53]
	ds_read_b128 v[116:119], v121 offset:26624
	s_waitcnt lgkmcnt(1)
	v_mfma_f32_16x16x32_f16 v[78:81], v[104:107], v[112:115], v[78:81]
	v_mfma_f32_16x16x32_f16 v[46:49], v[108:111], v[112:115], v[46:49]
	ds_read_b128 v[112:115], v121 offset:28672
	s_waitcnt lgkmcnt(1)
	v_mfma_f32_16x16x32_f16 v[74:77], v[104:107], v[116:119], v[74:77]
	v_mfma_f32_16x16x32_f16 v[42:45], v[108:111], v[116:119], v[42:45]
	ds_read_b128 v[116:119], v121 offset:30720
	s_waitcnt lgkmcnt(1)
	v_mfma_f32_16x16x32_f16 v[70:73], v[104:107], v[112:115], v[70:73]
	v_mfma_f32_16x16x32_f16 v[38:41], v[108:111], v[112:115], v[38:41]
	ds_read_b128 v[112:115], v121 offset:32768
	s_waitcnt lgkmcnt(1)
	v_mfma_f32_16x16x32_f16 v[66:69], v[104:107], v[116:119], v[66:69]
	v_mfma_f32_16x16x32_f16 v[34:37], v[108:111], v[116:119], v[34:37]
	ds_read_b128 v[116:119], v121 offset:34816
	s_waitcnt lgkmcnt(1)
	v_mfma_f32_16x16x32_f16 v[18:21], v[104:107], v[112:115], v[18:21]
	v_mfma_f32_16x16x32_f16 v[2:5], v[108:111], v[112:115], v[2:5]
	ds_read_b128 v[112:115], v121 offset:36864
	s_waitcnt lgkmcnt(1)
	v_mfma_f32_16x16x32_f16 v[26:29], v[104:107], v[116:119], v[26:29]
	v_mfma_f32_16x16x32_f16 v[10:13], v[108:111], v[116:119], v[10:13]
	ds_read_b128 v[116:119], v121 offset:38912
	s_waitcnt lgkmcnt(1)
	v_mfma_f32_16x16x32_f16 v[22:25], v[104:107], v[112:115], v[22:25]
	v_mfma_f32_16x16x32_f16 v[6:9], v[108:111], v[112:115], v[6:9]
	ds_read_b128 v[112:115], v122 offset:16384
	s_waitcnt lgkmcnt(1)
	v_mfma_f32_16x16x32_f16 v[30:33], v[104:107], v[116:119], v[30:33]
	v_mfma_f32_16x16x32_f16 v[14:17], v[108:111], v[116:119], v[14:17]
	ds_read_b128 v[116:119], v122 offset:18432
	ds_read_b128 v[104:107], v94 offset:0
	ds_read_b128 v[108:111], v94 offset:2048
	s_waitcnt lgkmcnt(0)
	v_mfma_f32_16x16x32_f16 v[124:127], v[104:107], v[112:115], v[124:127]
	v_mfma_f32_16x16x32_f16 v[62:65], v[108:111], v[112:115], v[62:65]
	ds_read_b128 v[112:115], v122 offset:20480
	s_waitcnt lgkmcnt(1)
	v_mfma_f32_16x16x32_f16 v[86:89], v[104:107], v[116:119], v[86:89]
	v_mfma_f32_16x16x32_f16 v[58:61], v[108:111], v[116:119], v[58:61]
	ds_read_b128 v[116:119], v122 offset:22528
	s_waitcnt lgkmcnt(1)
	v_mfma_f32_16x16x32_f16 v[96:99], v[104:107], v[112:115], v[96:99]
	v_mfma_f32_16x16x32_f16 v[54:57], v[108:111], v[112:115], v[54:57]
	ds_read_b128 v[112:115], v122 offset:24576
	s_waitcnt lgkmcnt(1)
	v_mfma_f32_16x16x32_f16 v[82:85], v[104:107], v[116:119], v[82:85]
	v_mfma_f32_16x16x32_f16 v[50:53], v[108:111], v[116:119], v[50:53]
	ds_read_b128 v[116:119], v122 offset:26624
	s_waitcnt lgkmcnt(1)
	v_mfma_f32_16x16x32_f16 v[78:81], v[104:107], v[112:115], v[78:81]
	v_mfma_f32_16x16x32_f16 v[46:49], v[108:111], v[112:115], v[46:49]
	ds_read_b128 v[112:115], v122 offset:28672
	s_waitcnt lgkmcnt(1)
	v_mfma_f32_16x16x32_f16 v[74:77], v[104:107], v[116:119], v[74:77]
	v_mfma_f32_16x16x32_f16 v[42:45], v[108:111], v[116:119], v[42:45]
	ds_read_b128 v[116:119], v122 offset:30720
	s_waitcnt lgkmcnt(1)
	v_mfma_f32_16x16x32_f16 v[70:73], v[104:107], v[112:115], v[70:73]
	v_mfma_f32_16x16x32_f16 v[38:41], v[108:111], v[112:115], v[38:41]
	ds_read_b128 v[112:115], v122 offset:32768
	s_waitcnt lgkmcnt(1)
	v_mfma_f32_16x16x32_f16 v[66:69], v[104:107], v[116:119], v[66:69]
	v_mfma_f32_16x16x32_f16 v[34:37], v[108:111], v[116:119], v[34:37]
	ds_read_b128 v[116:119], v122 offset:34816
	s_waitcnt lgkmcnt(1)
	v_mfma_f32_16x16x32_f16 v[18:21], v[104:107], v[112:115], v[18:21]
	v_mfma_f32_16x16x32_f16 v[2:5], v[108:111], v[112:115], v[2:5]
	ds_read_b128 v[112:115], v122 offset:36864
	s_waitcnt lgkmcnt(1)
	v_mfma_f32_16x16x32_f16 v[26:29], v[104:107], v[116:119], v[26:29]
	v_mfma_f32_16x16x32_f16 v[10:13], v[108:111], v[116:119], v[10:13]
	ds_read_b128 v[116:119], v122 offset:38912
	s_waitcnt lgkmcnt(0)
	s_barrier
	s_mov_b32 m0, s24
	s_nop 0
	global_load_lds_dwordx4 v100, s[36:37]
	s_mov_b32 m0, s25
	s_nop 0
	global_load_lds_dwordx4 v101, s[36:37]
	s_mov_b32 m0, s26
	s_nop 0
	global_load_lds_dwordx4 v102, s[36:37]
	s_mov_b32 m0, s27
	s_nop 0
	global_load_lds_dwordx4 v103, s[36:37]
	s_add_u32 s36, s36, 0x80
	s_addc_u32 s37, s37, 0
	s_mov_b32 m0, s28
	s_nop 0
	global_load_lds_dwordx4 v120, s[38:39]
	s_mov_b32 m0, s29
	s_nop 0
	global_load_lds_dwordx4 v120, s[46:47]
	s_mov_b32 m0, s30
	s_nop 0
	global_load_lds_dwordx4 v120, s[48:49]
	s_mov_b32 m0, s31
	s_nop 0
	global_load_lds_dwordx4 v120, s[50:51]
	s_mov_b32 m0, s32
	s_nop 0
	global_load_lds_dwordx4 v120, s[52:53]
	s_mov_b32 m0, s33
	s_nop 0
	global_load_lds_dwordx4 v120, s[54:55]
	s_add_u32 s38, s38, 0x80
	s_addc_u32 s39, s39, 0
	s_add_u32 s46, s46, 0x80
	s_addc_u32 s47, s47, 0
	s_add_u32 s48, s48, 0x80
	s_addc_u32 s49, s49, 0
	s_add_u32 s50, s50, 0x80
	s_addc_u32 s51, s51, 0
	s_add_u32 s52, s52, 0x80
	s_addc_u32 s53, s53, 0
	s_add_u32 s54, s54, 0x80
	s_addc_u32 s55, s55, 0
	s_waitcnt lgkmcnt(1)
	v_mfma_f32_16x16x32_f16 v[22:25], v[104:107], v[112:115], v[22:25]
	v_mfma_f32_16x16x32_f16 v[6:9], v[108:111], v[112:115], v[6:9]
	s_waitcnt lgkmcnt(0)
	v_mfma_f32_16x16x32_f16 v[30:33], v[104:107], v[116:119], v[30:33]
	v_mfma_f32_16x16x32_f16 v[14:17], v[108:111], v[116:119], v[14:17]
	s_waitcnt vmcnt(0)
	s_barrier
	ds_read_b128 v[104:107], v93 offset:0
	ds_read_b128 v[108:111], v93 offset:2048
	ds_read_b128 v[112:115], v121 offset:16384
	ds_read_b128 v[116:119], v121 offset:18432
	s_waitcnt lgkmcnt(1)
	v_mfma_f32_16x16x32_f16 v[124:127], v[104:107], v[112:115], v[124:127]
	v_mfma_f32_16x16x32_f16 v[62:65], v[108:111], v[112:115], v[62:65]
	ds_read_b128 v[112:115], v121 offset:20480
	s_waitcnt lgkmcnt(1)
	v_mfma_f32_16x16x32_f16 v[86:89], v[104:107], v[116:119], v[86:89]
	v_mfma_f32_16x16x32_f16 v[58:61], v[108:111], v[116:119], v[58:61]
	ds_read_b128 v[116:119], v121 offset:22528
	s_waitcnt lgkmcnt(1)
	v_mfma_f32_16x16x32_f16 v[96:99], v[104:107], v[112:115], v[96:99]
	v_mfma_f32_16x16x32_f16 v[54:57], v[108:111], v[112:115], v[54:57]
	ds_read_b128 v[112:115], v121 offset:24576
	s_waitcnt lgkmcnt(1)
	v_mfma_f32_16x16x32_f16 v[82:85], v[104:107], v[116:119], v[82:85]
	v_mfma_f32_16x16x32_f16 v[50:53], v[108:111], v[116:119], v[50:53]
	ds_read_b128 v[116:119], v121 offset:26624
	s_waitcnt lgkmcnt(1)
	v_mfma_f32_16x16x32_f16 v[78:81], v[104:107], v[112:115], v[78:81]
	v_mfma_f32_16x16x32_f16 v[46:49], v[108:111], v[112:115], v[46:49]
	ds_read_b128 v[112:115], v121 offset:28672
	s_waitcnt lgkmcnt(1)
	v_mfma_f32_16x16x32_f16 v[74:77], v[104:107], v[116:119], v[74:77]
	v_mfma_f32_16x16x32_f16 v[42:45], v[108:111], v[116:119], v[42:45]
	ds_read_b128 v[116:119], v121 offset:30720
	s_waitcnt lgkmcnt(1)
	v_mfma_f32_16x16x32_f16 v[70:73], v[104:107], v[112:115], v[70:73]
	v_mfma_f32_16x16x32_f16 v[38:41], v[108:111], v[112:115], v[38:41]
	ds_read_b128 v[112:115], v121 offset:32768
	s_waitcnt lgkmcnt(1)
	v_mfma_f32_16x16x32_f16 v[66:69], v[104:107], v[116:119], v[66:69]
	v_mfma_f32_16x16x32_f16 v[34:37], v[108:111], v[116:119], v[34:37]
	ds_read_b128 v[116:119], v121 offset:34816
	s_waitcnt lgkmcnt(1)
	v_mfma_f32_16x16x32_f16 v[18:21], v[104:107], v[112:115], v[18:21]
	v_mfma_f32_16x16x32_f16 v[2:5], v[108:111], v[112:115], v[2:5]
	ds_read_b128 v[112:115], v121 offset:36864
	s_waitcnt lgkmcnt(1)
	v_mfma_f32_16x16x32_f16 v[26:29], v[104:107], v[116:119], v[26:29]
	v_mfma_f32_16x16x32_f16 v[10:13], v[108:111], v[116:119], v[10:13]
	ds_read_b128 v[116:119], v121 offset:38912
	s_waitcnt lgkmcnt(1)
	v_mfma_f32_16x16x32_f16 v[22:25], v[104:107], v[112:115], v[22:25]
	v_mfma_f32_16x16x32_f16 v[6:9], v[108:111], v[112:115], v[6:9]
	ds_read_b128 v[112:115], v122 offset:16384
	s_waitcnt lgkmcnt(1)
	v_mfma_f32_16x16x32_f16 v[30:33], v[104:107], v[116:119], v[30:33]
	v_mfma_f32_16x16x32_f16 v[14:17], v[108:111], v[116:119], v[14:17]
	ds_read_b128 v[116:119], v122 offset:18432
	ds_read_b128 v[104:107], v94 offset:0
	ds_read_b128 v[108:111], v94 offset:2048
	s_waitcnt lgkmcnt(0)
	v_mfma_f32_16x16x32_f16 v[124:127], v[104:107], v[112:115], v[124:127]
	v_mfma_f32_16x16x32_f16 v[62:65], v[108:111], v[112:115], v[62:65]
	ds_read_b128 v[112:115], v122 offset:20480
	s_waitcnt lgkmcnt(1)
	v_mfma_f32_16x16x32_f16 v[86:89], v[104:107], v[116:119], v[86:89]
	v_mfma_f32_16x16x32_f16 v[58:61], v[108:111], v[116:119], v[58:61]
	ds_read_b128 v[116:119], v122 offset:22528
	s_waitcnt lgkmcnt(1)
	v_mfma_f32_16x16x32_f16 v[96:99], v[104:107], v[112:115], v[96:99]
	v_mfma_f32_16x16x32_f16 v[54:57], v[108:111], v[112:115], v[54:57]
	ds_read_b128 v[112:115], v122 offset:24576
	s_waitcnt lgkmcnt(1)
	v_mfma_f32_16x16x32_f16 v[82:85], v[104:107], v[116:119], v[82:85]
	v_mfma_f32_16x16x32_f16 v[50:53], v[108:111], v[116:119], v[50:53]
	ds_read_b128 v[116:119], v122 offset:26624
	s_waitcnt lgkmcnt(1)
	v_mfma_f32_16x16x32_f16 v[78:81], v[104:107], v[112:115], v[78:81]
	v_mfma_f32_16x16x32_f16 v[46:49], v[108:111], v[112:115], v[46:49]
	ds_read_b128 v[112:115], v122 offset:28672
	s_waitcnt lgkmcnt(1)
	v_mfma_f32_16x16x32_f16 v[74:77], v[104:107], v[116:119], v[74:77]
	v_mfma_f32_16x16x32_f16 v[42:45], v[108:111], v[116:119], v[42:45]
	ds_read_b128 v[116:119], v122 offset:30720
	s_waitcnt lgkmcnt(1)
	v_mfma_f32_16x16x32_f16 v[70:73], v[104:107], v[112:115], v[70:73]
	v_mfma_f32_16x16x32_f16 v[38:41], v[108:111], v[112:115], v[38:41]
	ds_read_b128 v[112:115], v122 offset:32768
	s_waitcnt lgkmcnt(1)
	v_mfma_f32_16x16x32_f16 v[66:69], v[104:107], v[116:119], v[66:69]
	v_mfma_f32_16x16x32_f16 v[34:37], v[108:111], v[116:119], v[34:37]
	ds_read_b128 v[116:119], v122 offset:34816
	s_waitcnt lgkmcnt(1)
	v_mfma_f32_16x16x32_f16 v[18:21], v[104:107], v[112:115], v[18:21]
	v_mfma_f32_16x16x32_f16 v[2:5], v[108:111], v[112:115], v[2:5]
	ds_read_b128 v[112:115], v122 offset:36864
	s_waitcnt lgkmcnt(1)
	v_mfma_f32_16x16x32_f16 v[26:29], v[104:107], v[116:119], v[26:29]
	v_mfma_f32_16x16x32_f16 v[10:13], v[108:111], v[116:119], v[10:13]
	ds_read_b128 v[116:119], v122 offset:38912
	s_waitcnt lgkmcnt(0)
	s_barrier
	s_waitcnt lgkmcnt(1)
	v_mfma_f32_16x16x32_f16 v[22:25], v[104:107], v[112:115], v[22:25]
	v_mfma_f32_16x16x32_f16 v[6:9], v[108:111], v[112:115], v[6:9]
	s_waitcnt lgkmcnt(0)
	v_mfma_f32_16x16x32_f16 v[30:33], v[104:107], v[116:119], v[30:33]
	v_mfma_f32_16x16x32_f16 v[14:17], v[108:111], v[116:119], v[14:17]
	s_nop 15
	s_nop 15
	s_movk_i32 s2, 0xfc
	v_cmp_gt_u32_e32 vcc, s2, v0
	s_mov_b32 s2, 0x12492493
	s_movk_i32 s4, 0x380
	s_movk_i32 s12, 0x110
	v_cmp_gt_u32_e64 s[4:5], s4, v0
	v_lshrrev_b32_e32 v93, 1, v0
	v_cndmask_b32_e32 v94, 0, v93, vcc
	s_nop 5
	v_cvt_f16_f32_e32 v86, v86
	s_nop 5
	v_cvt_f16_f32_e32 v54, v54
	v_cvt_f16_f32_e32 v82, v82
	v_cvt_f16_f32_e32 v50, v50
	s_nop 5
	v_cvt_f16_f32_e32 v78, v78
	v_mul_i32_i24_e32 v102, 0xffffffc2, v92
	v_mul_u32_u24_e32 v101, 0x110, v91
	v_lshlrev_b32_e32 v91, 6, v92
	v_add3_u32 v91, v91, v102, v101
	ds_write_b16 v91, v86 offset:32
	v_cvt_f16_f32_e32 v86, v87
	v_cvt_f16_f32_e32 v74, v74
	v_cvt_f16_f32_e32 v102, v125
	ds_write_b16 v91, v86 offset:304
	v_cvt_f16_f32_e32 v86, v88
	s_nop 2
	v_cvt_f16_f32_e32 v34, v34
	ds_write_b16 v91, v82 offset:96
	ds_write_b16 v91, v86 offset:576
	v_cvt_f16_f32_e32 v86, v89
	v_cvt_f16_f32_e32 v38, v38
	ds_write_b16 v91, v34 offset:4576
	ds_write_b16 v91, v86 offset:848
	v_cvt_f16_f32_e32 v86, v96
	s_nop 1
	v_cvt_f16_f32_e32 v62, v62
	v_cvt_f16_f32_e32 v34, v35
	s_nop 0
	v_cvt_f16_f32_e32 v58, v58
	ds_write_b16 v91, v38 offset:4544
	v_cvt_f16_f32_e32 v38, v39
	s_nop 1
	v_cvt_f16_f32_e32 v46, v46
	ds_write_b16 v91, v86 offset:64
	v_cvt_f16_f32_e32 v86, v97
	s_nop 0
	v_cvt_f16_f32_e32 v42, v42
	v_cvt_f16_f32_e32 v82, v83
	ds_write_b16 v91, v78 offset:128
	s_nop 1
	v_cvt_f16_f32_e32 v70, v70
	v_cvt_f16_f32_e32 v78, v79
	ds_write_b16 v91, v74 offset:160
	v_cvt_f16_f32_e32 v74, v75
	s_nop 0
	v_cvt_f16_f32_e32 v66, v66
	ds_write_b16 v91, v70 offset:192
	v_cvt_f16_f32_e32 v70, v71
	ds_write_b16 v91, v62 offset:4352
	ds_write_b16 v91, v66 offset:224
	v_cvt_f16_f32_e32 v66, v67
	v_cvt_f16_f32_e32 v62, v63
	ds_write_b16 v91, v58 offset:4384
	v_cvt_f16_f32_e32 v58, v59
	ds_write_b16 v91, v54 offset:4416
	v_cvt_f16_f32_e32 v54, v55
	ds_write_b16 v91, v50 offset:4448
	v_cvt_f16_f32_e32 v50, v51
	ds_write_b16 v91, v46 offset:4480
	v_cvt_f16_f32_e32 v46, v47
	ds_write_b16 v91, v42 offset:4512
	v_cvt_f16_f32_e32 v42, v43
	ds_write_b16 v91, v34 offset:4848
	v_cvt_f16_f32_e32 v34, v36
	ds_write_b16 v91, v38 offset:4816
	v_cvt_f16_f32_e32 v38, v40
	ds_write_b16 v91, v102 offset:272
	v_cvt_f16_f32_e32 v102, v126
	ds_write_b16 v91, v86 offset:336
	v_cvt_f16_f32_e32 v86, v98
	ds_write_b16 v91, v82 offset:368
	v_cvt_f16_f32_e32 v82, v84
	ds_write_b16 v91, v78 offset:400
	v_cvt_f16_f32_e32 v78, v80
	ds_write_b16 v91, v74 offset:432
	v_cvt_f16_f32_e32 v74, v76
	ds_write_b16 v91, v70 offset:464
	v_cvt_f16_f32_e32 v70, v72
	ds_write_b16 v91, v66 offset:496
	v_cvt_f16_f32_e32 v66, v68
	ds_write_b16 v91, v62 offset:4624
	v_cvt_f16_f32_e32 v62, v64
	ds_write_b16 v91, v58 offset:4656
	v_cvt_f16_f32_e32 v58, v60
	ds_write_b16 v91, v54 offset:4688
	v_cvt_f16_f32_e32 v54, v56
	ds_write_b16 v91, v50 offset:4720
	v_cvt_f16_f32_e32 v50, v52
	ds_write_b16 v91, v46 offset:4752
	v_cvt_f16_f32_e32 v46, v48
	ds_write_b16 v91, v42 offset:4784
	v_cvt_f16_f32_e32 v42, v44
	ds_write_b16 v91, v34 offset:5120
	v_cvt_f16_f32_e32 v34, v37
	ds_write_b16 v91, v38 offset:5088
	v_cvt_f16_f32_e32 v38, v41
	v_cvt_f16_f32_e32 v103, v124
	ds_write_b16 v91, v102 offset:544
	v_cvt_f16_f32_e32 v102, v127
	ds_write_b16 v91, v86 offset:608
	v_cvt_f16_f32_e32 v86, v99
	ds_write_b16 v91, v82 offset:640
	v_cvt_f16_f32_e32 v82, v85
	ds_write_b16 v91, v78 offset:672
	v_cvt_f16_f32_e32 v78, v81
	ds_write_b16 v91, v74 offset:704
	v_cvt_f16_f32_e32 v74, v77
	ds_write_b16 v91, v70 offset:736
	v_cvt_f16_f32_e32 v70, v73
	ds_write_b16 v91, v66 offset:768
	v_cvt_f16_f32_e32 v66, v69
	ds_write_b16 v91, v62 offset:4896
	v_cvt_f16_f32_e32 v62, v65
	ds_write_b16 v91, v58 offset:4928
	v_cvt_f16_f32_e32 v58, v61
	ds_write_b16 v91, v54 offset:4960
	v_cvt_f16_f32_e32 v54, v57
	ds_write_b16 v91, v50 offset:4992
	v_cvt_f16_f32_e32 v50, v53
	ds_write_b16 v91, v46 offset:5024
	v_cvt_f16_f32_e32 v46, v49
	ds_write_b16 v91, v42 offset:5056
	v_cvt_f16_f32_e32 v42, v45
	ds_write_b16 v91, v34 offset:5392
	v_min_u32_e32 v34, 8, v92
	v_mul_hi_u32 v100, v94, s2
	ds_write_b16 v91, v38 offset:5360
	v_cmp_gt_u32_e64 s[2:3], 9, v92
	v_mul_u32_u24_e32 v39, 14, v34
	v_and_b32_e32 v40, 48, v0
	v_lshlrev_b32_e32 v38, 2, v92
	ds_write_b16 v91, v103
	ds_write_b16 v91, v102 offset:816
	ds_write_b16 v91, v86 offset:880
	ds_write_b16 v91, v82 offset:912
	ds_write_b16 v91, v78 offset:944
	ds_write_b16 v91, v74 offset:976
	ds_write_b16 v91, v70 offset:1008
	ds_write_b16 v91, v66 offset:1040
	ds_write_b16 v91, v62 offset:5168
	ds_write_b16 v91, v58 offset:5200
	ds_write_b16 v91, v54 offset:5232
	ds_write_b16 v91, v50 offset:5264
	ds_write_b16 v91, v46 offset:5296
	ds_write_b16 v91, v42 offset:5328
	s_waitcnt lgkmcnt(0)
	s_barrier
	s_and_saveexec_b64 s[6:7], s[4:5]
	s_cbranch_execz .LBB1_9
	v_add_u32_e32 v34, v1, v39
	v_mad_u32_u24 v41, v34, s12, v40
	ds_read_b128 v[34:37], v41
	ds_read_b128 v[42:45], v41 offset:64
	ds_read_b128 v[46:49], v41 offset:128
	ds_read_b128 v[50:53], v41 offset:192
	v_cmp_ne_u32_e64 s[4:5], 3, v90
	v_mul_u32_u24_e32 v41, 9, v1
	s_and_b64 s[12:13], s[4:5], s[2:3]
	s_waitcnt lgkmcnt(1)
	v_mfma_f32_16x16x32_f16 v[34:37], v[34:37], v[46:49], 0
	s_waitcnt lgkmcnt(0)
	v_mfma_f32_16x16x32_f16 v[34:37], v[42:45], v[50:53], v[34:37]
	s_and_saveexec_b64 s[4:5], s[12:13]
	v_add_u32_e32 v42, v95, v41
	s_nop 5
	v_mul_f32_e32 v34, 0x3e000000, v34
	v_mad_u32_u24 v42, v42, 48, v38
	ds_write_b32 v42, v34 offset:34816
	s_or_b64 exec, exec, s[4:5]
	v_or_b32_e32 v34, 1, v95
	v_cmp_gt_u32_e64 s[4:5], 9, v34
	s_and_b64 s[12:13], s[4:5], s[2:3]
	s_and_saveexec_b64 s[4:5], s[12:13]
	v_add_u32_e32 v34, v34, v41
	v_mul_f32_e32 v35, 0x3e000000, v35
	v_mad_u32_u24 v34, v34, 48, v38
	ds_write_b32 v34, v35 offset:34816
	s_or_b64 exec, exec, s[4:5]
	v_or_b32_e32 v34, 2, v95
	v_cmp_gt_u32_e64 s[4:5], 9, v34
	s_and_b64 s[12:13], s[4:5], s[2:3]
	s_and_saveexec_b64 s[4:5], s[12:13]
	v_add_u32_e32 v34, v34, v41
	v_mul_f32_e32 v35, 0x3e000000, v36
	v_mad_u32_u24 v34, v34, 48, v38
	ds_write_b32 v34, v35 offset:34816
	s_or_b64 exec, exec, s[4:5]
	v_or_b32_e32 v34, 3, v95
	v_cmp_gt_u32_e64 s[4:5], 9, v34
	s_and_b64 s[4:5], s[4:5], s[2:3]
	s_and_b64 exec, exec, s[4:5]
	v_add_u32_e32 v34, v34, v41
	v_mul_f32_e32 v35, 0x3e000000, v37
	v_mad_u32_u24 v34, v34, 48, v38
	ds_write_b32 v34, v35 offset:34816
